# adds P9: the 4 slot->token loads per unit issued together (1 round trip instead of 4)
# baseline (speedup 1.0000x reference)
; template <class Epi, class Sched, bool ALIGN_EPI = false, bool SP2 = false, bool F8 = false, bool GATHER = false>
; __device__ __forceinline__ void gemm_phase(PG8_LAS unsigned char* lds, const Gemm g, const Sched& S, const Epi& E) {
;     ...
;     for (int i = 0; i < 2; ++i) { int R, C; stage_rc(tid * 16 + i * 8192, R, C); const int Rb = Epi::PERM ? ((R & ~31) + perm32(R & 31)) : R;
;         voffA[i] = (unsigned)(R * K + C) * 2u; voffB[i] = (unsigned)(Rb * K + C) * 2u; }
;     static_assert(!GATHER || SP2, "the gather form is written for the two-super-phase loop");
;     unsigned vo[2][2], nvo[2][2];
;     __device__ __forceinline__ int arow(const Unit& u, int R) const { const int e = u.pn / npn, base = (u.pm - tstart[e]) * 256, slot = base + R, cnt = tstart[40 + e];
;         if (tokof != nullptr) return slot < cnt ? tokof[e * 8192 + slot] : 0;
;         return u.pm * 256 + (slot < cnt ? R : cnt - 1 - base); }
.LBB0_969:
	s_andn2_b64 vcc, exec, s[4:5]
	s_cbranch_vccnz .LBB0_1003
	v_ashrrev_i32_e32 v2, 31, v6
	v_lshrrev_b32_e32 v2, 26, v2
	v_add_u32_e32 v2, v6, v2
	s_add_u32 s12, s30, 0x300000
	v_ashrrev_i32_e32 v4, 6, v2
	v_bfe_i32 v2, v6, 27, 1
	s_addc_u32 s13, s31, 0
	s_ashr_i32 s47, s46, 31
	v_lshlrev_b32_e32 v9, 4, v6
	v_lshrrev_b32_e32 v2, 22, v2
	s_lshr_b32 s1, s47, 28
	v_add_u32_e32 v2, v9, v2
	s_add_i32 s1, s46, s1
	v_and_b32_e32 v2, 0xfffffc00, v2
	s_ashr_i32 s1, s1, 4
	v_sub_u32_e32 v2, v9, v2
	s_lshl_b32 s2, s1, 2
	v_lshrrev_b32_e32 v3, 4, v2
	s_add_i32 s2, s2, 0
	v_bitop3_b32 v7, v3, v2, 32 bitop3:0x6c
	v_lshlrev_b32_e32 v2, 3, v4
	s_add_i32 s2, s2, 0x27400
	v_and_b32_e32 v8, -16, v2
	v_mov_b32_e32 v2, s2
	ds_read2_b32 v[2:3], v2 offset1:40
	v_ashrrev_i32_e32 v5, 31, v7
	v_lshrrev_b32_e32 v5, 26, v5
	v_add_u32_e32 v5, v7, v5
	v_ashrrev_i32_e32 v5, 6, v5
	s_waitcnt lgkmcnt(0)
	v_sub_u32_e32 v2, s62, v2
	v_add_u32_e32 v187, v5, v8
	v_lshlrev_b32_e32 v12, 8, v2
	v_add_u32_e32 v10, v12, v187
	s_lshl_b32 s1, s1, 13
	v_cmp_lt_i32_e32 vcc, v10, v3
	v_mov_b32_e32 v8, 0
	v_mov_b32_e32 v2, 0
	s_and_saveexec_b64 s[4:5], vcc
	s_cbranch_execz .LBB0_972
	v_add_u32_e32 v10, s1, v10
	v_ashrrev_i32_e32 v11, 31, v10
	v_lshl_add_u64 v[10:11], v[10:11], 2, s[12:13]
	global_load_dword v2, v[10:11], off
.LBB0_972:
	s_or_b64 exec, exec, s[4:5]
	v_add_u32_e32 v9, 0x2000, v9
	v_ashrrev_i32_e32 v10, 31, v9
	v_lshrrev_b32_e32 v10, 22, v10
	v_add_u32_e32 v10, v9, v10
	v_ashrrev_i32_e32 v10, 10, v10
	v_mul_i32_i24_e32 v11, 0x400, v10
	v_sub_u32_e32 v9, v9, v11
	v_lshrrev_b32_e32 v11, 4, v9
	v_bitop3_b32 v11, v11, v9, 32 bitop3:0x6c
	v_lshlrev_b32_e32 v9, 3, v10
	v_and_b32_e32 v13, -16, v9
	v_ashrrev_i32_e32 v9, 31, v11
	v_lshrrev_b32_e32 v9, 26, v9
	v_add_u32_e32 v9, v11, v9
	v_ashrrev_i32_e32 v9, 6, v9
	v_add_u32_e32 v188, v9, v13
	v_add_u32_e32 v13, v12, v188
	v_cmp_lt_i32_e32 vcc, v13, v3
	s_and_saveexec_b64 s[4:5], vcc
	s_cbranch_execz .LBB0_974
	v_add_u32_e32 v14, s1, v13
	v_ashrrev_i32_e32 v15, 31, v14
	v_lshl_add_u64 v[14:15], v[14:15], 2, s[12:13]
	global_load_dword v8, v[14:15], off
.LBB0_974:
	s_or_b64 exec, exec, s[4:5]
	v_add_u32_e32 v189, 0x80, v187
	v_add_u32_e32 v15, v12, v189
	v_cmp_lt_i32_e32 vcc, v15, v3
	v_mov_b32_e32 v13, 0
	v_mov_b32_e32 v14, 0
	v_mov_b32_e32 v16, 0
	s_and_saveexec_b64 s[4:5], vcc
	s_cbranch_execz .LBB0_976
	v_add_u32_e32 v14, s1, v15
	v_ashrrev_i32_e32 v15, 31, v14
	v_lshl_add_u64 v[14:15], v[14:15], 2, s[12:13]
	global_load_dword v14, v[14:15], off
.LBB0_976:
	s_or_b64 exec, exec, s[4:5]
	v_add_u32_e32 v191, 0x80, v188
	v_add_u32_e32 v12, v12, v191
	v_cmp_lt_i32_e32 vcc, v12, v3
	s_and_saveexec_b64 s[4:5], vcc
	s_cbranch_execz .LBB0_978
	v_add_u32_e32 v12, s1, v12
	v_ashrrev_i32_e32 v13, 31, v12
	v_lshl_add_u64 v[12:13], v[12:13], 2, s[12:13]
	global_load_dword v16, v[12:13], off
.LBB0_978:
	s_or_b64 exec, exec, s[4:5]
	s_waitcnt vmcnt(0)
	v_lshlrev_b32_e32 v2, 11, v2
	v_lshlrev_b32_e32 v8, 11, v8
	v_lshlrev_b32_e32 v14, 11, v14
	v_lshlrev_b32_e32 v13, 11, v16
	v_lshlrev_b32_e32 v3, 5, v4
	v_lshlrev_b32_e32 v4, 6, v5
	v_sub_u32_e32 v4, v7, v4
	v_mov_b32_e32 v7, 1
	v_ashrrev_i16_sdwa v4, v7, sext(v4) dst_sel:DWORD dst_unused:UNUSED_PAD src0_sel:DWORD src1_sel:BYTE_0
	v_and_b32_e32 v3, 32, v3
	v_bfe_i32 v4, v4, 0, 16
	v_add_lshl_u32 v192, v3, v4, 1
	v_lshlrev_b32_e32 v4, 6, v9
	v_sub_u32_e32 v4, v11, v4
	v_lshlrev_b32_e32 v3, 5, v10
	v_ashrrev_i16_sdwa v4, v7, sext(v4) dst_sel:DWORD dst_unused:UNUSED_PAD src0_sel:DWORD src1_sel:BYTE_0
	v_and_b32_e32 v3, 32, v3
	v_bfe_i32 v4, v4, 0, 16
	v_add_lshl_u32 v193, v3, v4, 1
	v_add_u32_e32 v162, v2, v192
	v_lshlrev_b32_e32 v2, 1, v187
	v_lshrrev_b32_e32 v3, 2, v187
	v_and_b32_e32 v4, 3, v5
	s_mov_b32 s1, 0x1fffe0
	v_and_b32_e32 v2, 24, v2
	v_and_b32_e32 v3, 4, v3
	v_and_or_b32 v4, v187, s1, v4
	v_or3_b32 v2, v4, v3, v2
	v_and_b32_e32 v4, 3, v9
	s_ashr_i32 s5, s40, 6
	s_lshl_b64 s[10:11], s[46:47], 19
	s_ashr_i32 s4, s40, 8
	v_and_or_b32 v4, v188, s1, v4
	s_lshl_b32 s1, s5, 10
	s_add_u32 s14, s30, 0x4000000
	s_addc_u32 s15, s31, 0
	s_add_u32 s2, s30, 0x44200000
	s_addc_u32 s3, s31, 0
	s_add_u32 s48, s2, s10
	v_lshl_add_u32 v164, v2, 11, v192
	v_lshlrev_b32_e32 v2, 1, v188
	v_lshrrev_b32_e32 v3, 2, v188
	s_addc_u32 s49, s3, s11
	s_add_i32 s9, s1, 0
	v_and_b32_e32 v2, 24, v2
	v_and_b32_e32 v3, 4, v3
	s_add_i32 m0, s9, 0x10000
	v_or3_b32 v2, v4, v3, v2
	global_load_lds_dwordx4 v164, s[48:49]
	s_add_i32 m0, s9, 0x12000
	v_lshl_add_u32 v166, v2, 11, v193
	s_add_u32 s10, s48, 0x40000
	global_load_lds_dwordx4 v166, s[48:49]
	s_addc_u32 s11, s49, 0
	s_add_i32 m0, s9, 0x14000
	v_add_u32_e32 v170, v8, v193
	global_load_lds_dwordx4 v164, s[10:11]
	s_add_i32 m0, s9, 0x16000
	v_add_u32_e32 v168, v14, v192
	global_load_lds_dwordx4 v166, s[10:11]
	s_mov_b32 m0, s9
	s_add_i32 s10, s9, 0x2000
	global_load_lds_dwordx4 v162, s[14:15]
	s_mov_b32 m0, s10
	s_add_i32 s11, s9, 0x4000
	global_load_lds_dwordx4 v170, s[14:15]
	s_mov_b32 m0, s11
	s_add_i32 s33, s9, 0x6000
	v_add_u32_e32 v172, v13, v193
	global_load_lds_dwordx4 v168, s[14:15]
	s_mov_b32 m0, s33
	v_mov_b32_e32 v163, 0
	global_load_lds_dwordx4 v172, s[14:15]
	v_mov_b32_e32 v165, v163
	v_mov_b32_e32 v167, v163
	s_cmp_eq_u32 s4, 1
	s_mov_b32 s34, 0
	v_lshl_add_u64 v[4:5], s[48:49], 0, v[164:165]
	v_lshl_add_u64 v[2:3], s[48:49], 0, v[166:167]
	s_cselect_b64 s[18:19], -1, 0
	s_cmp_lg_u32 s4, 1
	v_mov_b32_e32 v171, v163
	s_cbranch_scc1 .LBB0_980
	s_barrier

; #define PG8_SETVO(dst, u) do { _Pragma("unroll") for (int _h = 0; _h < 2; ++_h) _Pragma("unroll") for (int _i = 0; _i < 2; ++_i) { \
;         if constexpr (GATHER) { int R_, C_; stage_rc(tid * 16 + _i * 8192, R_, C_); dst[_h][_i] = (unsigned)(S.arow(u, R_ + HALF * _h) * K + C_) * 2u; } \
;         else dst[_h][_i] = voffA[_i] + (unsigned)_h * (unsigned)(HALF * K * 2); } } while (0)
; template <class Epi, class Sched, bool ALIGN_EPI = false, bool SP2 = false, bool F8 = false, bool GATHER = false>
; __device__ __forceinline__ void gemm_phase(PG8_LAS unsigned char* lds, const Gemm g, const Sched& S, const Epi& E) {
;     ...
;         const bool has_next = S.next(ui + 1, nxt);
;         const char* nA = (has_next && !GATHER) ? (const char*)g.A + (size_t)nxt.pm * tstep : cA; const char* nB = has_next ? (const char*)g.Bt + (size_t)nxt.pn * tstep : cB;
;         if (has_next) { PG8_SETVO(nvo, nxt); } else {
;     __device__ __forceinline__ int arow(const Unit& u, int R) const { const int e = u.pn / npn, base = (u.pm - tstart[e]) * 256, slot = base + R, cnt = tstart[40 + e];
;         if (tokof != nullptr) return slot < cnt ? tokof[e * 8192 + slot] : 0;
;         return u.pm * 256 + (slot < cnt ? R : cnt - 1 - base); }
.LBB0_985:
	v_cndmask_b32_e64 v2, 0, 1, s[50:51]
	v_cmp_ne_u32_e64 s[4:5], 1, v2
	s_andn2_b64 vcc, exec, s[50:51]
	v_mov_b32_e32 v202, v172
	v_mov_b32_e32 v201, v168
	v_mov_b32_e32 v203, v170
	v_mov_b32_e32 v204, v205
	s_cbranch_vccnz .LBB0_995
	s_ashr_i32 s43, s42, 31
	s_lshr_b32 s43, s43, 28
	s_add_i32 s43, s42, s43
	s_ashr_i32 s43, s43, 4
	s_lshl_b32 s44, s43, 2
	s_add_i32 s44, s44, 0
	s_add_i32 s44, s44, 0x27400
	v_mov_b32_e32 v2, s44
	ds_read2_b32 v[2:3], v2 offset1:40
	v_mov_b32_e32 v4, 0
	s_lshl_b32 s43, s43, 13
	s_waitcnt lgkmcnt(0)
	v_sub_u32_e32 v2, s61, v2
	v_lshlrev_b32_e32 v5, 8, v2
	v_add_u32_e32 v6, v5, v187
	v_cmp_lt_i32_e32 vcc, v6, v3
	v_mov_b32_e32 v2, 0
	s_and_saveexec_b64 s[44:45], vcc
	s_cbranch_execz .LBB0_988
	v_add_u32_e32 v6, s43, v6
	v_ashrrev_i32_e32 v7, 31, v6
	v_lshl_add_u64 v[6:7], v[6:7], 2, s[12:13]
	global_load_dword v2, v[6:7], off
.LBB0_988:
	s_or_b64 exec, exec, s[44:45]
	v_add_u32_e32 v6, v5, v188
	v_cmp_lt_i32_e32 vcc, v6, v3
	s_and_saveexec_b64 s[44:45], vcc
	s_cbranch_execz .LBB0_990
	v_add_u32_e32 v6, s43, v6
	v_ashrrev_i32_e32 v7, 31, v6
	v_lshl_add_u64 v[6:7], v[6:7], 2, s[12:13]
	global_load_dword v4, v[6:7], off
.LBB0_990:
	s_or_b64 exec, exec, s[44:45]
	v_add_u32_e32 v8, v5, v189
	v_cmp_lt_i32_e32 vcc, v8, v3
	v_mov_b32_e32 v6, 0
	v_mov_b32_e32 v7, 0
	s_and_saveexec_b64 s[44:45], vcc
	s_cbranch_execz .LBB0_992
	v_add_u32_e32 v8, s43, v8
	v_ashrrev_i32_e32 v9, 31, v8
	v_lshl_add_u64 v[8:9], v[8:9], 2, s[12:13]
	global_load_dword v7, v[8:9], off
.LBB0_992:
	s_or_b64 exec, exec, s[44:45]
	v_add_u32_e32 v5, v5, v191
	v_cmp_lt_i32_e32 vcc, v5, v3
	s_and_saveexec_b64 s[44:45], vcc
	s_cbranch_execz .LBB0_994
	v_add_u32_e32 v8, s43, v5
	v_ashrrev_i32_e32 v9, 31, v8
	v_lshl_add_u64 v[8:9], v[8:9], 2, s[12:13]
	global_load_dword v6, v[8:9], off
.LBB0_994:
	s_or_b64 exec, exec, s[44:45]
	s_waitcnt vmcnt(0)
	v_lshlrev_b32_e32 v2, 11, v2
	v_lshlrev_b32_e32 v4, 11, v4
	v_lshlrev_b32_e32 v7, 11, v7
	v_lshlrev_b32_e32 v6, 11, v6
	v_add_u32_e32 v201, v7, v192
	v_add_u32_e32 v203, v4, v193
	v_add_u32_e32 v204, v2, v192
	v_add_u32_e32 v202, v6, v193
